# attention phases P3-P5: waves 4-7 run at s_setprio 1 (static priority for the later-dispatched half)
# speedup vs baseline: 1.0037x; 1.0029x over previous
; #define LAS __attribute__((address_space(3)))
; __device__ __forceinline__ void fresh_tid(Ctx& C) { int t = threadIdx.x; asm volatile("" : "+v"(t)); C.tid = t; C.lane = t & 63; const Args* k = C.ka; asm volatile("" : "+s"(k)); C.ka = k; }
; #define REP(k) if ((MK_REPEAT >> (k)) & 1)
; #define IN(k) (fresh_tid(C), lo <= (k) && (k) < hi)
; #define SEAM(k) do { if (IN(k) && IN((k) + 1)) xcd_barrier(bar); } while (0)
;     const int w = C.wave, lane = C.lane, i = lane & 15, g4 = lane >> 4, tid = C.tid;
;     LAS unsigned char* lds = C.lds;
;     LAS unsigned* MASK = (LAS unsigned*)(lds + 131072);
;     LAS int* USED = (LAS int*)(lds + LDS_MISC + 512);
;     LAS int* WCNT = (LAS int*)(lds + LDS_MISC + 512 + 1024);
;     const float mb = WSP(float, WS_MISC)[64];
;     const bf16_t* Kall = WSP(bf16_t, MODE == MODE_SEL ? WS_KSEL : WS_KWIN); const bf16_t* VTall = WSP(bf16_t, MODE == MODE_SEL ? WS_VSELT : WS_VWINT);
;     constexpr int NT = 4 * 256;
;     for (int it = C.bid; it < NT; it += C.G) {
;         const int round = it / C.G, base = C.G * round, cntr = (NT - base) < C.G ? (NT - base) : C.G, off = it - base;
;         const int tk = base + ((round & 1) ? cntr - 1 - off : off);
;         const int qt = 255 - (tk >> 2), bg = tk & 3, b = bg >> 1, g = bg & 1, t0 = 64 * qt;
; __global__ void __launch_bounds__(512, 2) mk_fwd(Args args) {
;     ...
;     if (IN(3)) { tile_attn_phase<MODE_WIN>(C); REP(3) { tile_attn_phase<MODE_WIN>(C); } fresh_tid(C); for (int rep_ = 0; rep_ < 1 + ((MK_REPEAT >> 13) & 1); ++rep_) xattn_tiled(C); fresh_tid(C); p3_tasks(C); REP(4) { xcd_barrier(bar); p3_tasks(C); } } SEAM(3);
.LBB0_426:
	s_cmp_lt_i32 s72, 4
	s_cselect_b64 s[0:1], -1, 0
	v_writelane_b32 v254, s72, 13
	s_cmp_gt_i32 s73, 3
	s_cselect_b64 s[2:3], -1, 0
	v_mov_b32_e32 v2, v0
	s_and_b64 s[0:1], s[0:1], s[2:3]
	v_writelane_b32 v254, s73, 14
	v_cndmask_b32_e64 v1, 0, 1, s[0:1]
	v_cmp_ne_u32_e64 s[4:5], 1, v1
	s_andn2_b64 vcc, exec, s[0:1]
	s_mov_b64 s[84:85], s[56:57]
	v_readlane_b32 s57, v254, 12
	s_cbranch_vccnz .LBB0_488
	v_readlane_b32 s0, v254, 4
	s_nop 0
	s_cmpk_lt_u32 s0, 0x100
	s_cbranch_scc1 .Lprio_lo
	s_setprio 1
.Lprio_lo:
	v_readlane_b32 s0, v254, 0
	s_cmpk_lt_i32 s0, 0x400
	v_readlane_b32 s1, v254, 1
	s_cbranch_scc1 .LBB0_429
	s_lshl_b32 s22, s57, 3
	s_lshl_b32 s25, s57, 4
	s_lshl_b32 s0, s57, 2
	s_or_b32 s24, s22, 4
	s_or_b32 s21, s25, 8
	s_and_b32 s23, s0, 12
	s_lshl_b32 s18, s57, 11
	s_lshl_b32 s19, s24, 8
	s_lshl_b32 s20, s21, 7
	s_cbranch_execz .LBB0_430
	s_branch .LBB0_448
